# attn normed stores nt (on top of wo nt)
# baseline (speedup 1.0000x reference)
.Ll2_post:
	ds_read_b128 v[66:69], v189
	ds_read_b128 v[70:73], v189 offset:1152
	s_addk_i32 s11, 0x7c0
	s_and_b32 s0, s11, 0x7c0
	s_lshl_b32 s0, s0, 2
	s_mov_b32 s1, 0
	v_lshl_add_u64 v[74:75], v[174:175], 0, s[0:1]
	s_waitcnt lgkmcnt(1)
	global_store_dwordx4 v[74:75], v[66:69], off nt
	s_mov_b32 s0, 0x10800
	v_lshlrev_b32_e32 v1, 2, v1
	v_add_co_u32_e32 v66, vcc, 0x10000, v74
	v_lshrrev_b32_e32 v86, 2, v0
	s_nop 0
	v_addc_co_u32_e32 v67, vcc, 0, v75, vcc
	s_waitcnt lgkmcnt(0)
	global_store_dwordx4 v[66:67], v[70:73], off nt
	ds_read_b128 v[66:69], v189 offset:2304
	ds_read_b128 v[70:73], v189 offset:3456
	v_add_co_u32_e32 v76, vcc, 0x20000, v74
	v_lshlrev_b32_e32 v0, 5, v0
	s_nop 0
	v_addc_co_u32_e32 v77, vcc, 0, v75, vcc
	s_waitcnt lgkmcnt(1)
	global_store_dwordx4 v[76:77], v[66:69], off nt
	v_and_b32_e32 v87, 0x60, v0
	v_lshlrev_b32_e32 v88, 2, v87
	v_add_co_u32_e32 v66, vcc, 0x30000, v74
	s_nop 1
	v_addc_co_u32_e32 v67, vcc, 0, v75, vcc
	s_waitcnt lgkmcnt(0)
	global_store_dwordx4 v[66:67], v[70:73], off nt
	v_lshl_or_b32 v67, v182, 2, v183
	v_mad_u32_u24 v66, v184, s0, 0
	v_mul_u32_u24_e32 v67, 0x210, v67
	v_add3_u32 v1, v66, v1, v67
	s_barrier
	ds_write2_b32 v1, v50, v34 offset1:32
	ds_write2_b32 v1, v51, v35 offset0:132 offset1:164
	v_add_u32_e32 v34, 0x400, v1
	ds_write2_b32 v34, v52, v36 offset0:8 offset1:40
	ds_write2_b32 v34, v53, v37 offset0:140 offset1:172
	v_add_u32_e32 v35, 0x1000, v1
	v_add_u32_e32 v36, 0x1400, v1
	ds_write2_b32 v35, v54, v38 offset0:32 offset1:64
	ds_write2_b32 v35, v55, v39 offset0:164 offset1:196
	ds_write2_b32 v36, v56, v40 offset0:40 offset1:72
	ds_write2_b32 v36, v57, v41 offset0:172 offset1:204
	v_add_u32_e32 v37, 0x2000, v1
	v_add_u32_e32 v38, 0x2400, v1
	v_add_u32_e32 v40, 0x3200, v1
	ds_write2_b32 v37, v58, v42 offset0:64 offset1:96
	ds_write2_b32 v37, v59, v43 offset0:196 offset1:228
	ds_write2_b32 v38, v60, v44 offset0:72 offset1:104
	ds_write2_b32 v38, v61, v45 offset0:204 offset1:236
	v_add_u32_e32 v39, 0x3000, v1
	ds_write2_b32 v40, v63, v47 offset0:100 offset1:132
	v_add_u32_e32 v40, 0x3400, v1
	v_add_u32_e32 v41, 0x3600, v1
	ds_write2_b32 v39, v62, v46 offset0:96 offset1:128
	ds_write2_b32 v40, v64, v48 offset0:104 offset1:136
	ds_write2_b32 v41, v65, v49 offset0:108 offset1:140
	ds_write2_b32 v1, v18, v2 offset0:64 offset1:96
	ds_write2_b32 v1, v19, v3 offset0:196 offset1:228
	ds_write2_b32 v34, v20, v4 offset0:72 offset1:104
	ds_write2_b32 v34, v21, v5 offset0:204 offset1:236
	ds_write2_b32 v35, v22, v6 offset0:96 offset1:128
	v_add_u32_e32 v2, 0x1200, v1
	ds_write2_b32 v2, v23, v7 offset0:100 offset1:132
	ds_write2_b32 v36, v24, v8 offset0:104 offset1:136
	v_add_u32_e32 v2, 0x1600, v1
	ds_write2_b32 v2, v25, v9 offset0:108 offset1:140
	ds_write2_b32 v37, v26, v10 offset0:128 offset1:160
	ds_write2_b32 v38, v27, v11 offset0:4 offset1:36
	ds_write2_b32 v38, v28, v12 offset0:136 offset1:168
	v_add_u32_e32 v2, 0x2800, v1
	v_add_u32_e32 v1, 0x3800, v1
	ds_write2_b32 v2, v29, v13 offset0:12 offset1:44
	ds_write2_b32 v39, v30, v14 offset0:160 offset1:192
	ds_write2_b32 v40, v31, v15 offset0:36 offset1:68
	ds_write2_b32 v40, v32, v16 offset0:168 offset1:200
	ds_write2_b32 v1, v33, v17 offset0:44 offset1:76
	v_mul_u32_u24_e32 v1, 0x210, v86
	v_add3_u32 v89, 0, v1, v88
	v_add_u32_e32 v0, 0x10800, v89
	s_waitcnt lgkmcnt(0)
	s_barrier
	ds_read_b128 v[10:13], v0
	ds_read_b128 v[14:17], v0 offset:16
	ds_read_b128 v[4:7], v89 offset:16
	ds_read_b128 v[18:21], v89
	v_add_u32_e32 v26, 0x10820, v89
	ds_read_b128 v[22:25], v89 offset:32
	ds_read_b128 v[0:3], v89 offset:48
	v_add_u32_e32 v34, 0x10810, v89
	s_waitcnt lgkmcnt(3)
	v_pk_add_f32 v[16:17], v[6:7], v[16:17]
	v_pk_add_f32 v[14:15], v[4:5], v[14:15]
	s_waitcnt lgkmcnt(2)
	v_pk_add_f32 v[10:11], v[18:19], v[10:11]
	v_pk_add_f32 v[8:9], v[20:21], v[12:13]
	v_pk_mul_f32 v[20:21], v[16:17], v[16:17]
	v_pk_mul_f32 v[16:17], v[10:11], v[10:11]
	v_pk_mul_f32 v[14:15], v[14:15], v[14:15]
	v_pk_mul_f32 v[12:13], v[8:9], v[8:9]
	v_mov_b32_e32 v18, v16
	v_mov_b32_e32 v19, v14
	v_mov_b32_e32 v14, v17
	v_pk_add_f32 v[14:15], v[18:19], v[14:15]
	v_mov_b32_e32 v16, v12
	v_mov_b32_e32 v17, v20
	v_pk_add_f32 v[18:19], v[14:15], v[16:17]
	v_mov_b32_e32 v20, v13
	ds_read_b128 v[14:17], v26 offset:16
	v_pk_add_f32 v[12:13], v[18:19], v[20:21]
	ds_read_b128 v[18:21], v26
	v_add_u32_e32 v38, 0x10840, v89
	ds_read_b128 v[26:29], v38
	s_waitcnt lgkmcnt(2)
	v_pk_add_f32 v[32:33], v[0:1], v[14:15]
	v_pk_add_f32 v[30:31], v[2:3], v[16:17]
	s_waitcnt lgkmcnt(1)
	v_pk_add_f32 v[80:81], v[22:23], v[18:19]
	v_pk_add_f32 v[78:79], v[24:25], v[20:21]
	v_pk_mul_f32 v[18:19], v[80:81], v[80:81]
	v_pk_mul_f32 v[22:23], v[32:33], v[32:33]
	v_pk_mul_f32 v[20:21], v[78:79], v[78:79]
	v_pk_mul_f32 v[30:31], v[30:31], v[30:31]
	v_mov_b32_e32 v24, v18
	v_mov_b32_e32 v25, v22
	v_mov_b32_e32 v22, v19
	v_pk_add_f32 v[18:19], v[24:25], v[22:23]
	v_mov_b32_e32 v22, v20
	v_mov_b32_e32 v23, v30
	ds_read_b128 v[14:17], v34
	v_pk_add_f32 v[32:33], v[18:19], v[22:23]
	v_mov_b32_e32 v30, v21
	ds_read_b128 v[18:21], v89 offset:80
	ds_read_b128 v[22:25], v38 offset:16
	v_pk_add_f32 v[82:83], v[32:33], v[30:31]
	ds_read_b128 v[30:33], v89 offset:64
	ds_read_b128 v[34:37], v89 offset:80
	ds_read_b128 v[38:41], v38
	ds_read_b128 v[42:45], v89 offset:64
	v_add_u32_e32 v74, 0x10860, v89
	s_waitcnt lgkmcnt(4)
	v_pk_add_f32 v[20:21], v[20:21], v[24:25]
	v_pk_add_f32 v[18:19], v[18:19], v[22:23]
	s_waitcnt lgkmcnt(3)
	v_pk_add_f32 v[22:23], v[30:31], v[26:27]
	v_pk_add_f32 v[24:25], v[32:33], v[28:29]
	v_pk_mul_f32 v[28:29], v[20:21], v[20:21]
	v_pk_mul_f32 v[20:21], v[22:23], v[22:23]
	v_pk_mul_f32 v[30:31], v[18:19], v[18:19]
	v_pk_mul_f32 v[26:27], v[24:25], v[24:25]
	v_mov_b32_e32 v32, v20
	v_mov_b32_e32 v33, v30
	v_mov_b32_e32 v30, v21
	global_load_dwordx4 v[18:21], v88, s[8:9] offset:16
	global_load_dwordx4 v[22:25], v88, s[8:9]
	v_pk_add_f32 v[30:31], v[32:33], v[30:31]
	v_mov_b32_e32 v32, v26
	v_mov_b32_e32 v33, v28
	v_pk_add_f32 v[30:31], v[30:31], v[32:33]
	v_mov_b32_e32 v28, v27
	v_pk_add_f32 v[84:85], v[30:31], v[28:29]
	ds_read_b128 v[26:29], v89 offset:96
	ds_read_b128 v[30:33], v89 offset:112
	ds_read_b128 v[46:49], v74
	ds_read_b128 v[50:53], v74 offset:16
	global_load_dwordx4 v[54:57], v88, s[8:9] offset:48
	global_load_dwordx4 v[58:61], v88, s[8:9] offset:32
	v_add_u32_e32 v62, 0x10830, v89
	ds_read_b128 v[62:65], v62
	ds_read_b128 v[66:69], v89 offset:112
	s_waitcnt lgkmcnt(3)
	v_pk_add_f32 v[28:29], v[28:29], v[48:49]
	s_waitcnt lgkmcnt(2)
	v_pk_add_f32 v[30:31], v[30:31], v[50:51]
	v_pk_add_f32 v[26:27], v[26:27], v[46:47]
	v_pk_mul_f32 v[46:47], v[28:29], v[28:29]
	v_pk_mul_f32 v[26:27], v[26:27], v[26:27]
	v_pk_mul_f32 v[28:29], v[30:31], v[30:31]
	v_pk_add_f32 v[32:33], v[32:33], v[52:53]
	v_mov_b32_e32 v30, v26
	v_mov_b32_e32 v31, v28
	v_mov_b32_e32 v28, v27
	ds_read_b128 v[70:73], v89 offset:96
	ds_read_b128 v[74:77], v74
	v_pk_mul_f32 v[48:49], v[32:33], v[32:33]
	v_pk_add_f32 v[50:51], v[30:31], v[28:29]
	global_load_dwordx4 v[26:29], v88, s[8:9] offset:80
	global_load_dwordx4 v[30:33], v88, s[8:9] offset:64
	v_add_f32_e32 v12, v12, v13
	v_add_f32_e32 v12, v12, v82
	v_mov_b32_e32 v52, v46
	v_mov_b32_e32 v53, v48
	v_add_f32_e32 v12, v12, v83
	v_pk_add_f32 v[50:51], v[50:51], v[52:53]
	v_mov_b32_e32 v48, v47
	v_add_f32_e32 v12, v12, v84
	v_pk_add_f32 v[46:47], v[50:51], v[48:49]
	v_add_f32_e32 v12, v12, v85
	v_add_f32_e32 v12, v12, v46
	v_add_f32_e32 v12, v12, v47
	global_load_dwordx4 v[46:49], v88, s[8:9] offset:96
	global_load_dwordx4 v[50:53], v88, s[8:9] offset:112
	ds_bpermute_b32 v13, v181, v12
	s_mov_b32 s0, 0x800000
	v_pk_add_f32 v[4:5], v[4:5], v[14:15]
	s_waitcnt lgkmcnt(4)
	v_pk_add_f32 v[0:1], v[0:1], v[62:63]
	s_waitcnt lgkmcnt(0)
	v_add_f32_e32 v12, v12, v13
	ds_bpermute_b32 v13, v180, v12
	s_waitcnt lgkmcnt(0)
	v_add_f32_e32 v12, v12, v13
	v_mov_b32_e32 v13, 0x3727c5ac
	v_fmac_f32_e32 v13, 0x3c000000, v12
	v_mul_f32_e32 v12, 0x4b800000, v13
	v_cmp_gt_f32_e32 vcc, s0, v13
	s_lshl_b32 s0, s12, 1
	s_nop 0
	v_cndmask_b32_e32 v12, v13, v12, vcc
	v_rsq_f32_e32 v12, v12
	s_nop 0
	v_mul_f32_e32 v13, 0x45800000, v12
	v_cndmask_b32_e32 v12, v12, v13, vcc
	v_mul_f32_e32 v82, 0x3f4ccccd, v12
	v_add_u32_e32 v12, s16, v86
	v_mov_b32_e32 v13, 0
	v_lshlrev_b64 v[84:85], 12, v[12:13]
	v_lshl_add_u64 v[84:85], s[6:7], 0, v[84:85]
	v_pk_mul_f32 v[4:5], v[82:83], v[4:5] op_sel_hi:[0,1]
	v_lshl_add_u64 v[84:85], v[84:85], 0, s[0:1]
	v_lshlrev_b32_e32 v12, 1, v87
	v_lshl_add_u64 v[84:85], v[84:85], 0, v[12:13]
	v_pk_mul_f32 v[0:1], v[82:83], v[0:1] op_sel_hi:[0,1]
	v_pk_mul_f32 v[10:11], v[82:83], v[10:11] op_sel_hi:[0,1]
	v_pk_mul_f32 v[8:9], v[82:83], v[8:9] op_sel_hi:[0,1]
	s_waitcnt vmcnt(7)
	v_pk_mul_f32 v[4:5], v[4:5], v[18:19]
	s_nop 0
	v_cvt_pk_f16_f32 v12, v4, v5
	v_pk_add_f32 v[4:5], v[6:7], v[16:17]
	v_pk_mul_f32 v[6:7], v[82:83], v[78:79] op_sel_hi:[0,1]
	v_pk_mul_f32 v[4:5], v[82:83], v[4:5] op_sel_hi:[0,1]
	v_pk_mul_f32 v[4:5], v[4:5], v[20:21]
	s_waitcnt vmcnt(6)
	v_pk_mul_f32 v[10:11], v[10:11], v[22:23]
	v_cvt_pk_f16_f32 v13, v4, v5
	v_pk_mul_f32 v[4:5], v[82:83], v[80:81] op_sel_hi:[0,1]
	s_waitcnt vmcnt(4)
	v_pk_mul_f32 v[4:5], v[4:5], v[58:59]
	v_pk_mul_f32 v[6:7], v[6:7], v[60:61]
	v_pk_mul_f32 v[0:1], v[0:1], v[54:55]
	v_cvt_pk_f16_f32 v4, v4, v5
	v_cvt_pk_f16_f32 v5, v6, v7
	v_cvt_pk_f16_f32 v6, v0, v1
	v_pk_add_f32 v[0:1], v[2:3], v[64:65]
	v_pk_add_f32 v[2:3], v[44:45], v[40:41]
	v_pk_mul_f32 v[0:1], v[82:83], v[0:1] op_sel_hi:[0,1]
	v_pk_mul_f32 v[0:1], v[0:1], v[56:57]
	v_pk_mul_f32 v[8:9], v[8:9], v[24:25]
	v_cvt_pk_f16_f32 v7, v0, v1
	global_store_dwordx4 v[84:85], v[4:7], off offset:16 nt
	v_pk_add_f32 v[0:1], v[42:43], v[38:39]
	v_cvt_pk_f16_f32 v10, v10, v11
	v_add_u32_e32 v4, 0x10850, v89
	v_pk_mul_f32 v[6:7], v[82:83], v[2:3] op_sel_hi:[0,1]
	ds_read_b128 v[2:5], v4
	v_pk_mul_f32 v[0:1], v[82:83], v[0:1] op_sel_hi:[0,1]
	s_waitcnt vmcnt(3)
	v_pk_mul_f32 v[0:1], v[0:1], v[30:31]
	v_pk_mul_f32 v[6:7], v[6:7], v[32:33]
	v_cvt_pk_f16_f32 v0, v0, v1
	v_cvt_pk_f16_f32 v1, v6, v7
	v_add_u32_e32 v6, 0x10870, v89
	v_cvt_pk_f16_f32 v11, v8, v9
	ds_read_b128 v[6:9], v6
	s_waitcnt lgkmcnt(1)
	v_pk_add_f32 v[2:3], v[34:35], v[2:3]
	v_pk_add_f32 v[4:5], v[36:37], v[4:5]
	v_pk_mul_f32 v[2:3], v[82:83], v[2:3] op_sel_hi:[0,1]
	v_pk_mul_f32 v[4:5], v[82:83], v[4:5] op_sel_hi:[0,1]
	v_pk_mul_f32 v[2:3], v[2:3], v[26:27]
	v_pk_mul_f32 v[4:5], v[4:5], v[28:29]
	v_cvt_pk_f16_f32 v2, v2, v3
	v_cvt_pk_f16_f32 v3, v4, v5
	global_store_dwordx4 v[84:85], v[0:3], off offset:32 nt
	s_waitcnt lgkmcnt(0)
	v_pk_add_f32 v[4:5], v[68:69], v[8:9]
	global_store_dwordx4 v[84:85], v[10:13], off nt
	v_pk_add_f32 v[0:1], v[70:71], v[74:75]
	v_pk_add_f32 v[2:3], v[72:73], v[76:77]
	v_pk_mul_f32 v[0:1], v[82:83], v[0:1] op_sel_hi:[0,1]
	v_pk_mul_f32 v[2:3], v[82:83], v[2:3] op_sel_hi:[0,1]
	s_waitcnt vmcnt(4)
	v_pk_mul_f32 v[0:1], v[0:1], v[46:47]
	v_pk_mul_f32 v[2:3], v[2:3], v[48:49]
	v_cvt_pk_f16_f32 v0, v0, v1
	v_cvt_pk_f16_f32 v1, v2, v3
	v_pk_add_f32 v[2:3], v[66:67], v[6:7]
	v_pk_mul_f32 v[4:5], v[82:83], v[4:5] op_sel_hi:[0,1]
	v_pk_mul_f32 v[2:3], v[82:83], v[2:3] op_sel_hi:[0,1]
	s_waitcnt vmcnt(3)
	v_pk_mul_f32 v[2:3], v[2:3], v[50:51]
	v_pk_mul_f32 v[4:5], v[4:5], v[52:53]
	v_cvt_pk_f16_f32 v2, v2, v3
	v_cvt_pk_f16_f32 v3, v4, v5
	global_store_dwordx4 v[84:85], v[0:3], off offset:48 nt
	s_endpgm
